# v3 + P9 sink lane table + next-item K/V band prefetch issued before the QK^T part instead of after it
# speedup vs baseline: 1.0029x; 1.0029x over previous
.LBB0_869:
	s_ashr_i32 s38, s37, 31
	s_lshr_b32 s2, s38, 25
	s_add_i32 s2, s37, s2
	s_ashr_i32 s39, s2, 7
	s_lshr_b32 s2, s39, 30
	s_add_i32 s2, s39, s2
	s_and_b32 s2, s2, 0x3ffffffc
	s_sub_i32 s2, s39, s2
	s_lshl_b32 s2, s2, 2
	s_or_b32 s8, s2, s22
	s_mul_i32 s2, s34, 0xd000
	s_ashr_i32 s9, s8, 31
	s_add_i32 s36, s2, 0
	s_add_i32 s35, s37, s72
	s_add_i32 s2, s8, 16
	s_nop 3
	v_readlane_b32 s3, v255, s2
	s_nop 1
	v_mov_b32_e32 v156, s3
	s_cmpk_gt_i32 s35, 0xfff
	s_cbranch_scc1 .Lp9_kvdone
	s_ashr_i32 s2, s35, 31
	s_lshr_b32 s3, s2, 23
	s_lshr_b32 s2, s2, 25
	s_add_i32 s2, s35, s2
	s_ashr_i32 s6, s2, 7
	s_add_i32 s3, s35, s3
	s_lshr_b32 s2, s6, 30
	s_ashr_i32 s14, s3, 9
	s_add_i32 s2, s6, s2
	s_lshl_b32 s9, s6, 13
	s_and_b32 s2, s2, -4
	s_ashr_i32 s15, s14, 31
	s_sub_i32 s16, s6, s2
	s_lshl_b64 s[2:3], s[14:15], 22
	s_add_u32 s40, s18, s2
	s_addc_u32 s41, s19, s3
	s_lshl_b32 s16, s16, 6
	s_ashr_i32 s17, s16, 31
	s_lshl_b64 s[2:3], s[16:17], 1
	s_add_u32 s2, s40, s2
	s_addc_u32 s3, s41, s3
	v_mov_b32_e32 v137, v112
	v_lshl_add_u64 v[118:119], s[2:3], 0, v[136:137]
	s_sub_i32 s2, s30, s9
	v_mov_b32_e32 v113, v112
	v_add_u32_e32 v84, s2, v152
	v_mov_b32_e32 v114, v112
	v_mov_b32_e32 v115, v112
	v_mov_b64_e32 v[80:81], v[112:113]
	v_cmp_lt_i32_e32 vcc, -1, v84
	v_mov_b64_e32 v[82:83], v[114:115]
	s_and_saveexec_b64 s[2:3], vcc
	s_cbranch_execz .LBB0_872
	v_mov_b32_e32 v85, v112
	v_lshlrev_b64 v[80:81], 9, v[84:85]
	v_lshl_add_u64 v[80:81], v[118:119], 0, v[80:81]
	global_load_dwordx4 v[80:83], v[80:81], off

.Lp9_kvdone:
	s_lshl_b32 s2, s8, 9
	s_add_i32 s2, s2, 0
	v_mov_b32_e32 v157, v123
	s_add_i32 s2, s2, 0x1a000
	v_add3_u32 v113, s36, v140, v144
	v_lshl_add_u32 v74, v157, 2, s2
	ds_read2_b32 v[2:3], v74 offset0:127 offset1:128
	ds_read2_b32 v[4:5], v74 offset0:125 offset1:126
	ds_read2_b32 v[6:7], v74 offset0:119 offset1:120
	ds_read2_b32 v[8:9], v74 offset0:117 offset1:118
	ds_read2_b32 v[10:11], v74 offset0:111 offset1:112
	ds_read2_b32 v[12:13], v74 offset0:109 offset1:110
	ds_read2_b32 v[14:15], v74 offset0:103 offset1:104
	ds_read2_b32 v[20:21], v74 offset0:101 offset1:102
	ds_read_b128 v[16:19], v113
	s_waitcnt lgkmcnt(8)
	v_mov_b32_e32 v0, v3
	v_mov_b32_e32 v1, v2
	s_waitcnt lgkmcnt(7)
	v_mov_b32_e32 v2, v5
	v_mov_b32_e32 v3, v4
	s_waitcnt lgkmcnt(6)
	v_mov_b32_e32 v4, v7
	v_mov_b32_e32 v5, v6
	s_waitcnt lgkmcnt(5)
	v_mov_b32_e32 v6, v9
	v_mov_b32_e32 v7, v8
	s_waitcnt lgkmcnt(4)
	v_mov_b32_e32 v8, v11
	v_mov_b32_e32 v9, v10
	s_waitcnt lgkmcnt(3)
	v_mov_b32_e32 v10, v13
	v_mov_b32_e32 v11, v12
	s_waitcnt lgkmcnt(2)
	v_mov_b32_e32 v12, v15
	v_mov_b32_e32 v13, v14
	s_waitcnt lgkmcnt(1)
	v_mov_b32_e32 v14, v21
	v_mov_b32_e32 v15, v20
	ds_read_b128 v[20:23], v113 offset:32
	v_subrev_u32_e32 v72, 44, v74
	s_waitcnt lgkmcnt(1)
	v_mfma_f32_32x32x16_bf16 v[0:15], v[16:19], v[92:95], v[0:15]
	v_add_u32_e32 v78, 0xffffff9c, v74
	v_add_u32_e32 v135, 0xffffff94, v74
	s_cmpk_lt_i32 s35, 0x1000
	s_cselect_b64 s[12:13], -1, 0
	s_cmpk_gt_i32 s35, 0xfff
	s_cselect_b64 s[10:11], -1, 0
	s_and_b64 vcc, exec, s[10:11]
	s_waitcnt lgkmcnt(0)
	v_mfma_f32_32x32x16_bf16 v[0:15], v[20:23], v[96:99], v[0:15]
	ds_read_b128 v[16:19], v113 offset:64
	ds_read_b128 v[20:23], v113 offset:96
	s_waitcnt lgkmcnt(1)
	v_mfma_f32_32x32x16_bf16 v[0:15], v[16:19], v[100:103], v[0:15]
	s_waitcnt lgkmcnt(0)
	v_mfma_f32_32x32x16_bf16 v[0:15], v[20:23], v[104:107], v[0:15]
	ds_read2_b32 v[18:19], v74 offset0:95 offset1:96
	ds_read2_b32 v[20:21], v74 offset0:93 offset1:94
	ds_read2_b32 v[22:23], v74 offset0:87 offset1:88
	ds_read2_b32 v[24:25], v74 offset0:85 offset1:86
	ds_read2_b32 v[26:27], v74 offset0:79 offset1:80
	ds_read2_b32 v[28:29], v74 offset0:77 offset1:78
	ds_read2_b32 v[30:31], v74 offset0:71 offset1:72
	ds_read2_b32 v[36:37], v74 offset0:69 offset1:70
	ds_read_b128 v[32:35], v113 offset:4608
	s_waitcnt lgkmcnt(8)
	v_mov_b32_e32 v16, v19
	v_mov_b32_e32 v17, v18
	s_waitcnt lgkmcnt(7)
	v_mov_b32_e32 v18, v21
	v_mov_b32_e32 v19, v20
	s_waitcnt lgkmcnt(6)
	v_mov_b32_e32 v20, v23
	v_mov_b32_e32 v21, v22
	s_waitcnt lgkmcnt(5)
	v_mov_b32_e32 v22, v25
	v_mov_b32_e32 v23, v24
	s_waitcnt lgkmcnt(4)
	v_mov_b32_e32 v24, v27
	v_mov_b32_e32 v25, v26
	s_waitcnt lgkmcnt(3)
	v_mov_b32_e32 v26, v29
	v_mov_b32_e32 v27, v28
	s_waitcnt lgkmcnt(2)
	v_mov_b32_e32 v28, v31
	v_mov_b32_e32 v29, v30
	s_waitcnt lgkmcnt(1)
	v_mov_b32_e32 v30, v37
	v_mov_b32_e32 v31, v36
	ds_read_b128 v[36:39], v113 offset:4640
	s_waitcnt lgkmcnt(1)
	v_mfma_f32_32x32x16_bf16 v[16:31], v[32:35], v[92:95], v[16:31]
	s_waitcnt lgkmcnt(0)
	v_mfma_f32_32x32x16_bf16 v[16:31], v[36:39], v[96:99], v[16:31]
	ds_read_b128 v[32:35], v113 offset:4672
	ds_read_b128 v[36:39], v113 offset:4704
	s_waitcnt lgkmcnt(1)
	v_mfma_f32_32x32x16_bf16 v[16:31], v[32:35], v[100:103], v[16:31]
	s_waitcnt lgkmcnt(0)
	v_mfma_f32_32x32x16_bf16 v[16:31], v[36:39], v[104:107], v[16:31]
	ds_read2_b32 v[34:35], v74 offset0:63 offset1:64
	ds_read2_b32 v[36:37], v74 offset0:61 offset1:62
	ds_read2_b32 v[38:39], v74 offset0:55 offset1:56
	ds_read2_b32 v[40:41], v74 offset0:53 offset1:54
	ds_read2_b32 v[42:43], v74 offset0:47 offset1:48
	ds_read2_b32 v[44:45], v74 offset0:45 offset1:46
	ds_read2_b32 v[46:47], v74 offset0:39 offset1:40
	ds_read2_b32 v[52:53], v74 offset0:37 offset1:38
	ds_read_b128 v[48:51], v113 offset:9216
	s_waitcnt lgkmcnt(8)
	v_mov_b32_e32 v32, v35
	v_mov_b32_e32 v33, v34
	s_waitcnt lgkmcnt(7)
	v_mov_b32_e32 v34, v37
	v_mov_b32_e32 v35, v36
	s_waitcnt lgkmcnt(6)
	v_mov_b32_e32 v36, v39
	v_mov_b32_e32 v37, v38
	s_waitcnt lgkmcnt(5)
	v_mov_b32_e32 v38, v41
	v_mov_b32_e32 v39, v40
	s_waitcnt lgkmcnt(4)
	v_mov_b32_e32 v40, v43
	v_mov_b32_e32 v41, v42
	s_waitcnt lgkmcnt(3)
	v_mov_b32_e32 v42, v45
	v_mov_b32_e32 v43, v44
	s_waitcnt lgkmcnt(2)
	v_mov_b32_e32 v44, v47
	v_mov_b32_e32 v45, v46
	s_waitcnt lgkmcnt(1)
	v_mov_b32_e32 v46, v53
	v_mov_b32_e32 v47, v52
	ds_read_b128 v[52:55], v113 offset:9248
	s_waitcnt lgkmcnt(1)
	v_mfma_f32_32x32x16_bf16 v[32:47], v[48:51], v[92:95], v[32:47]
	s_waitcnt lgkmcnt(0)
	v_mfma_f32_32x32x16_bf16 v[32:47], v[52:55], v[96:99], v[32:47]
	ds_read_b128 v[48:51], v113 offset:9280
	ds_read_b128 v[52:55], v113 offset:9312
	s_waitcnt lgkmcnt(1)
	v_mfma_f32_32x32x16_bf16 v[32:47], v[48:51], v[100:103], v[32:47]
	s_waitcnt lgkmcnt(0)
	v_mfma_f32_32x32x16_bf16 v[32:47], v[52:55], v[104:107], v[32:47]
	ds_read2_b32 v[50:51], v74 offset0:31 offset1:32
	ds_read2_b32 v[52:53], v74 offset0:29 offset1:30
	ds_read2_b32 v[54:55], v74 offset0:23 offset1:24
	ds_read2_b32 v[56:57], v74 offset0:21 offset1:22
	ds_read2_b32 v[58:59], v74 offset0:15 offset1:16
	ds_read2_b32 v[60:61], v74 offset0:13 offset1:14
	ds_read2_b32 v[62:63], v74 offset0:7 offset1:8
	ds_read2_b32 v[68:69], v74 offset0:5 offset1:6
	ds_read_b128 v[64:67], v113 offset:13824
	s_waitcnt lgkmcnt(8)
	v_mov_b32_e32 v48, v51
	v_mov_b32_e32 v49, v50
	s_waitcnt lgkmcnt(7)
	v_mov_b32_e32 v50, v53
	v_mov_b32_e32 v51, v52
	s_waitcnt lgkmcnt(6)
	v_mov_b32_e32 v52, v55
	v_mov_b32_e32 v53, v54
	s_waitcnt lgkmcnt(5)
	v_mov_b32_e32 v54, v57
	v_mov_b32_e32 v55, v56
	s_waitcnt lgkmcnt(4)
	v_mov_b32_e32 v56, v59
	v_mov_b32_e32 v57, v58
	s_waitcnt lgkmcnt(3)
	v_mov_b32_e32 v58, v61
	v_mov_b32_e32 v59, v60
	s_waitcnt lgkmcnt(2)
	v_mov_b32_e32 v60, v63
	v_mov_b32_e32 v61, v62
	s_waitcnt lgkmcnt(1)
	v_mov_b32_e32 v62, v69
	v_mov_b32_e32 v63, v68
	ds_read_b128 v[68:71], v113 offset:13856
	s_waitcnt lgkmcnt(1)
	v_mfma_f32_32x32x16_bf16 v[48:63], v[64:67], v[92:95], v[48:63]
	s_waitcnt lgkmcnt(0)
	v_mfma_f32_32x32x16_bf16 v[48:63], v[68:71], v[96:99], v[48:63]
	ds_read_b128 v[64:67], v113 offset:13888
	ds_read_b128 v[68:71], v113 offset:13920
	s_waitcnt lgkmcnt(1)
	v_mfma_f32_32x32x16_bf16 v[48:63], v[64:67], v[100:103], v[48:63]
	v_add_u32_e32 v64, -4, v74
	v_add_u32_e32 v65, -12, v74
	s_waitcnt lgkmcnt(0)
	v_mfma_f32_32x32x16_bf16 v[48:63], v[68:71], v[104:107], v[48:63]
	v_subrev_u32_e32 v70, 36, v74
	ds_read2_b32 v[66:67], v64 offset1:1
	ds_read2_b32 v[68:69], v65 offset1:1
	ds_read2_b32 v[70:71], v70 offset1:1
	ds_read2_b32 v[72:73], v72 offset1:1
	v_add_u32_e32 v64, 0xffffffbc, v74
	v_add_u32_e32 v65, 0xffffffb4, v74
	ds_read2_b32 v[74:75], v64 offset1:1
	ds_read2_b32 v[76:77], v65 offset1:1
	ds_read2_b32 v[78:79], v78 offset1:1
	ds_read2_b32 v[138:139], v135 offset1:1
	ds_read_b128 v[158:161], v113 offset:18432
	ds_read_b128 v[162:165], v113 offset:18464
	s_waitcnt lgkmcnt(9)
	v_mov_b32_e32 v64, v67
	v_mov_b32_e32 v65, v66
	s_waitcnt lgkmcnt(8)
	v_mov_b32_e32 v66, v69
	v_mov_b32_e32 v67, v68
	s_waitcnt lgkmcnt(7)
	v_mov_b32_e32 v68, v71
	v_mov_b32_e32 v69, v70
	s_waitcnt lgkmcnt(6)
	v_mov_b32_e32 v70, v73
	v_mov_b32_e32 v71, v72
	s_waitcnt lgkmcnt(5)
	v_mov_b32_e32 v72, v75
	v_mov_b32_e32 v73, v74
	s_waitcnt lgkmcnt(4)
	v_mov_b32_e32 v74, v77
	v_mov_b32_e32 v75, v76
	s_waitcnt lgkmcnt(3)
	v_mov_b32_e32 v76, v79
	v_mov_b32_e32 v77, v78
	s_waitcnt lgkmcnt(2)
	v_mov_b32_e32 v78, v139
	v_mov_b32_e32 v79, v138
	s_waitcnt lgkmcnt(1)
	s_nop 0
	v_mfma_f32_32x32x16_bf16 v[64:79], v[158:161], v[92:95], v[64:79]
	s_waitcnt lgkmcnt(0)
	v_mfma_f32_32x32x16_bf16 v[64:79], v[162:165], v[96:99], v[64:79]
	ds_read_b128 v[158:161], v113 offset:18496
	ds_read_b128 v[162:165], v113 offset:18528
	s_waitcnt lgkmcnt(1)
	v_mfma_f32_32x32x16_bf16 v[64:79], v[158:161], v[100:103], v[64:79]
	s_waitcnt lgkmcnt(0)
	v_mfma_f32_32x32x16_bf16 v[64:79], v[162:165], v[104:107], v[64:79]
	s_cbranch_vccnz .LBB0_885
	s_ashr_i32 s2, s35, 31
	s_lshr_b32 s3, s2, 23
	s_lshr_b32 s2, s2, 25
	s_add_i32 s2, s35, s2
	s_ashr_i32 s6, s2, 7
	s_add_i32 s3, s35, s3
	s_lshr_b32 s2, s6, 30
	s_ashr_i32 s14, s3, 9
	s_add_i32 s2, s6, s2
	s_lshl_b32 s9, s6, 13
	s_add_i32 s17, s23, s30
	s_and_b32 s2, s2, -4
	s_ashr_i32 s15, s14, 31
	s_sub_i32 s17, s17, s9
	s_sub_i32 s16, s6, s2
	s_lshl_b64 s[2:3], s[14:15], 13
	s_ashr_i32 s40, s17, 31
	s_add_u32 s2, s2, s17
	s_addc_u32 s3, s3, s40
	v_mov_b32_e32 v139, s3
	v_or_b32_e32 v138, s2, v122
	s_lshl_b32 s2, s16, 8
	v_lshlrev_b64 v[138:139], 11, v[138:139]
	s_or_b32 s2, s2, s26
	v_lshl_add_u64 v[138:139], s[4:5], 0, v[138:139]
	s_ashr_i32 s3, s2, 31
	v_lshl_add_u64 v[138:139], s[2:3], 1, v[138:139]
	v_mov_b32_e32 v135, v112
	v_lshl_add_u64 v[138:139], v[138:139], 0, v[134:135]
	global_load_dwordx4 v[92:95], v[138:139], off
	global_load_dwordx4 v[96:99], v[138:139], off offset:32
	global_load_dwordx4 v[100:103], v[138:139], off offset:64
	global_load_dwordx4 v[104:107], v[138:139], off offset:96
